# speedup vs baseline: 1.0066x; 1.0066x over previous
.LBB1_74:
	s_cmp_lt_u32 s50, 2
	s_cbranch_scc1 .Lfin0_skip
	v_add_u32_e32 v100, s44, v209
	ds_read_b64_tr_b16 v[178:179], v100 offset:24576
	ds_read_b64_tr_b16 v[180:181], v100 offset:25088
	v_add_f32_e32 v82, v66, v67
	v_add_f32_e32 v82, v68, v82
	v_add_f32_e32 v82, v69, v82
	v_add_f32_e32 v82, v70, v82
	v_add_f32_e32 v98, v71, v82
	s_waitcnt lgkmcnt(9)
	v_mfma_f32_32x32x16_f16 v[82:97], v[174:177], v[142:145], v[34:49]
	v_cvt_pk_f16_f32 v134, v66, v67
	v_cvt_pk_f16_f32 v135, v68, v69
	ds_read_b64_tr_b16 v[174:175], v100 offset:28672
	ds_read_b64_tr_b16 v[176:177], v100 offset:29184
	s_waitcnt lgkmcnt(10)
	v_mfma_f32_32x32x16_f16 v[34:49], v[170:173], v[142:145], v[34:49]
	v_add_f32_e32 v66, v72, v98
	v_add_f32_e32 v66, v73, v66
	v_add_f32_e32 v66, v74, v66
	v_add_f32_e32 v66, v75, v66
	v_cvt_pk_f16_f32 v136, v70, v71
	v_cvt_pk_f16_f32 v137, v72, v73
	ds_read_b64_tr_b16 v[170:171], v100 offset:25600
	ds_read_b64_tr_b16 v[172:173], v100 offset:26112
	s_waitcnt lgkmcnt(11)
	v_mfma_f32_32x32x16_f16 v[82:97], v[166:169], v[138:141], v[82:97]
	v_add_f32_e32 v66, v76, v66
	v_add_f32_e32 v66, v77, v66
	v_add_f32_e32 v66, v78, v66
	v_add_f32_e32 v66, v79, v66
	v_cvt_pk_f16_f32 v126, v74, v75
	v_cvt_pk_f16_f32 v127, v76, v77
	ds_read_b64_tr_b16 v[142:143], v100 offset:29696
	ds_read_b64_tr_b16 v[144:145], v100 offset:30208
	s_waitcnt lgkmcnt(12)
	v_mfma_f32_32x32x16_f16 v[34:49], v[162:165], v[138:141], v[34:49]
	v_add_f32_e32 v66, v80, v66
	v_add_f32_e32 v66, v81, v66
	v_add_f32_e32 v66, v50, v66
	v_add_f32_e32 v66, v51, v66
	v_cvt_pk_f16_f32 v128, v78, v79
	v_cvt_pk_f16_f32 v129, v80, v81
	ds_read_b64_tr_b16 v[110:111], v100 offset:26624
	ds_read_b64_tr_b16 v[112:113], v100 offset:27136
	s_waitcnt lgkmcnt(13)
	v_mfma_f32_32x32x16_f16 v[82:97], v[158:161], v[130:133], v[82:97]
	v_add_f32_e32 v66, v52, v66
	v_add_f32_e32 v66, v53, v66
	v_add_f32_e32 v66, v54, v66
	v_add_f32_e32 v66, v55, v66
	v_cvt_pk_f16_f32 v118, v50, v51
	v_cvt_pk_f16_f32 v119, v52, v53
	ds_read_b64_tr_b16 v[106:107], v100 offset:30720
	ds_read_b64_tr_b16 v[108:109], v100 offset:31232
	s_waitcnt lgkmcnt(14)
	v_mfma_f32_32x32x16_f16 v[34:49], v[154:157], v[130:133], v[34:49]
	v_add_f32_e32 v50, v56, v66
	v_add_f32_e32 v50, v57, v50
	v_add_f32_e32 v50, v58, v50
	v_add_f32_e32 v50, v59, v50
	v_cvt_pk_f16_f32 v120, v54, v55
	v_cvt_pk_f16_f32 v121, v56, v57
	ds_read_b64_tr_b16 v[102:103], v100 offset:27648
	ds_read_b64_tr_b16 v[104:105], v100 offset:28160
	s_waitcnt lgkmcnt(14)
	v_mfma_f32_32x32x16_f16 v[82:97], v[150:153], v[122:125], v[82:97]
	v_add_f32_e32 v50, v60, v50
	v_add_f32_e32 v50, v61, v50
	v_add_f32_e32 v50, v62, v50
	v_add_f32_e32 v50, v63, v50
	v_cvt_pk_f16_f32 v114, v58, v59
	v_cvt_pk_f16_f32 v115, v60, v61
	ds_read_b64_tr_b16 v[98:99], v100 offset:31744
	ds_read_b64_tr_b16 v[100:101], v100 offset:32256
	v_mfma_f32_32x32x16_f16 v[34:49], v[146:149], v[122:125], v[34:49]
	v_add_f32_e32 v50, v64, v50
	v_add_f32_e32 v50, v65, v50
	v_add_f32_e32 v66, 0, v50
	v_cvt_pk_f16_f32 v116, v62, v63
	v_cvt_pk_f16_f32 v117, v64, v65
	s_cmp_lt_u32 s50, 3
	s_cbranch_scc1 .Lmfill_0f
	v_or_b32_e32 v214, 0xe0, v210
	v_or_b32_e32 v213, 0xc0, v210
	v_mov_b32_e32 v67, 0xff800000
	v_cmp_le_u32_e32 vcc, v214, v204
	v_or_b32_e32 v215, 0xe1, v210
	v_or_b32_e32 v216, 0xc2, v210
	s_nop 0
	v_cndmask_b32_e32 v34, v67, v34, vcc
	v_cmp_lt_u32_e32 vcc, v213, v204
	v_or_b32_e32 v217, 0xe2, v210
	v_or_b32_e32 v218, 0xc3, v210
	v_cndmask_b32_e32 v51, v67, v83, vcc
	v_cmp_le_u32_e32 vcc, v213, v204
	v_or_b32_e32 v219, 0xe3, v210
	v_or_b32_e32 v220, 0xc8, v210
	v_cndmask_b32_e32 v50, v67, v82, vcc
	v_cmp_le_u32_e32 vcc, v215, v204
	v_or_b32_e32 v221, 0xe8, v210
	v_or_b32_e32 v222, 0xc9, v210
	v_cndmask_b32_e32 v35, v67, v35, vcc
	v_cmp_le_u32_e32 vcc, v216, v204
	v_or_b32_e32 v223, 0xe9, v210
	v_or_b32_e32 v224, 0xca, v210
	v_cndmask_b32_e32 v52, v67, v84, vcc
	v_cmp_le_u32_e32 vcc, v217, v204
	v_or_b32_e32 v225, 0xea, v210
	v_or_b32_e32 v226, 0xcb, v210
	v_cndmask_b32_e32 v36, v67, v36, vcc
	v_cmp_le_u32_e32 vcc, v218, v204
	v_or_b32_e32 v227, 0xeb, v210
	v_or_b32_e32 v228, 0xd0, v210
	v_cndmask_b32_e32 v53, v67, v85, vcc
	v_cmp_le_u32_e32 vcc, v219, v204
	v_or_b32_e32 v229, 0xf0, v210
	v_or_b32_e32 v230, 0xd1, v210
	v_cndmask_b32_e32 v37, v67, v37, vcc
	v_cmp_le_u32_e32 vcc, v220, v204
	v_or_b32_e32 v231, 0xf1, v210
	v_or_b32_e32 v232, 0xd2, v210
	v_cndmask_b32_e32 v54, v67, v86, vcc
	v_cmp_le_u32_e32 vcc, v221, v204
	v_or_b32_e32 v233, 0xf2, v210
	v_or_b32_e32 v234, 0xd3, v210
	v_cndmask_b32_e32 v38, v67, v38, vcc
	v_cmp_le_u32_e32 vcc, v222, v204
	v_or_b32_e32 v235, 0xf3, v210
	v_or_b32_e32 v236, 0xd8, v210
	v_cndmask_b32_e32 v55, v67, v87, vcc
	v_cmp_le_u32_e32 vcc, v223, v204
	v_or_b32_e32 v237, 0xf8, v210
	v_or_b32_e32 v238, 0xd9, v210
	v_cndmask_b32_e32 v39, v67, v39, vcc
	v_cmp_le_u32_e32 vcc, v224, v204
	v_or_b32_e32 v239, 0xf9, v210
	v_or_b32_e32 v240, 0xda, v210
	v_cndmask_b32_e32 v56, v67, v88, vcc
	v_cmp_le_u32_e32 vcc, v225, v204
	v_or_b32_e32 v241, 0xfa, v210
	v_or_b32_e32 v242, 0xdb, v210
	v_cndmask_b32_e32 v40, v67, v40, vcc
	v_cmp_le_u32_e32 vcc, v226, v204
	v_or_b32_e32 v243, 0xfb, v210
	v_max_f32_e32 v68, v50, v50
	v_cndmask_b32_e32 v57, v67, v89, vcc
	v_cmp_le_u32_e32 vcc, v227, v204
	v_add_f32_e32 v82, v203, v66
	s_mov_b32 s2, 0x41000000
	v_cndmask_b32_e32 v41, v67, v41, vcc
	v_cmp_le_u32_e32 vcc, v228, v204
	s_nop 1
	v_cndmask_b32_e32 v58, v67, v90, vcc
	v_cmp_le_u32_e32 vcc, v229, v204
	s_nop 1
	v_cndmask_b32_e32 v42, v67, v42, vcc
	v_cmp_le_u32_e32 vcc, v230, v204
	s_nop 1
	v_cndmask_b32_e32 v59, v67, v91, vcc
	v_cmp_le_u32_e32 vcc, v231, v204
	s_nop 1
	v_cndmask_b32_e32 v43, v67, v43, vcc
	v_cmp_le_u32_e32 vcc, v232, v204
	s_nop 1
	v_cndmask_b32_e32 v60, v67, v92, vcc
	v_cmp_le_u32_e32 vcc, v233, v204
	s_nop 1
	v_cndmask_b32_e32 v44, v67, v44, vcc
	v_cmp_le_u32_e32 vcc, v234, v204
	s_nop 1
	v_cndmask_b32_e32 v61, v67, v93, vcc
	v_cmp_le_u32_e32 vcc, v235, v204
	s_nop 1
	v_cndmask_b32_e32 v45, v67, v45, vcc
	v_cmp_le_u32_e32 vcc, v236, v204
	s_nop 1
	v_cndmask_b32_e32 v62, v67, v94, vcc
	v_cmp_le_u32_e32 vcc, v237, v204
	s_nop 1
	v_cndmask_b32_e32 v46, v67, v46, vcc
	v_cmp_le_u32_e32 vcc, v238, v204
	s_nop 1
	v_cndmask_b32_e32 v63, v67, v95, vcc
	v_cmp_le_u32_e32 vcc, v239, v204
	s_nop 1
	v_cndmask_b32_e32 v47, v67, v47, vcc
	v_cmp_le_u32_e32 vcc, v240, v204
	s_nop 1
	v_cndmask_b32_e32 v64, v67, v96, vcc
	v_cmp_le_u32_e32 vcc, v241, v204
	s_nop 1
	v_cndmask_b32_e32 v48, v67, v48, vcc
	v_cmp_le_u32_e32 vcc, v242, v204
	s_nop 1
	v_cndmask_b32_e32 v65, v67, v97, vcc
	v_cmp_le_u32_e32 vcc, v243, v204
	s_nop 1
	v_cndmask_b32_e32 v49, v67, v49, vcc

.Lfin0_land:
	s_cbranch_scc1 .LBB1_79
	s_lshl_b32 s2, s30, 8
	s_ashr_i32 s16, s2, 31
	s_add_u32 s2, s2, s29
	s_addc_u32 s16, s16, 0
	s_add_u32 s2, s2, s37
	s_addc_u32 s16, s16, 0
	s_mulk_i32 s16, 0xe00
	s_mul_hi_u32 s17, s2, 0xe00
	s_add_i32 s17, s17, s16
	s_mulk_i32 s2, 0xe00
	s_add_u32 s4, s4, s2
	s_addc_u32 s5, s5, s17
	s_lshl_b32 s2, s36, 6
	s_lshl_b64 s[2:3], s[2:3], 1
	s_add_u32 s2, s4, s2
	s_addc_u32 s3, s5, s3
	v_lshlrev_b32_e32 v68, 1, v190
	v_mov_b32_e32 v69, 0
	v_lshl_add_u64 v[68:69], s[2:3], 0, v[68:69]
	global_load_dwordx4 v[140:143], v[68:69], off
	v_lshl_add_u64 v[70:71], v[68:69], 0, 32
	global_load_dwordx4 v[136:139], v[70:71], off
	v_lshl_add_u64 v[70:71], v[68:69], 0, 64
	global_load_dwordx4 v[132:135], v[70:71], off
	s_mov_b64 s[2:3], 0x60
	v_lshl_add_u64 v[68:69], v[68:69], 0, s[2:3]
	global_load_dwordx4 v[128:131], v[68:69], off
	s_branch .LBB1_80

.LBB1_103:
	s_cmp_lt_u32 s50, 2
	s_cbranch_scc1 .Lfin1_skip
	v_add_u32_e32 v65, s26, v251
	ds_read_b64_tr_b16 v[124:125], v65
	ds_read_b64_tr_b16 v[126:127], v65 offset:512
	s_waitcnt lgkmcnt(9)
	v_mfma_f32_32x32x16_f16 v[96:111], v[188:191], v[140:143], v[32:47]
	v_add_f32_e32 v66, v80, v81
	v_add_f32_e32 v66, v82, v66
	v_add_f32_e32 v66, v83, v66
	v_add_f32_e32 v66, v84, v66
	v_add_f32_e32 v66, v85, v66
	v_cvt_pk_f16_f32 v156, v80, v81
	v_cvt_pk_f16_f32 v157, v82, v83
	ds_read_b64_tr_b16 v[120:121], v65 offset:4096
	ds_read_b64_tr_b16 v[122:123], v65 offset:4608
	s_waitcnt lgkmcnt(10)
	v_mfma_f32_32x32x16_f16 v[32:47], v[184:187], v[140:143], v[32:47]
	v_add_f32_e32 v66, v86, v66
	v_add_f32_e32 v66, v87, v66
	v_add_f32_e32 v66, v88, v66
	v_add_f32_e32 v66, v89, v66
	v_cvt_pk_f16_f32 v158, v84, v85
	v_cvt_pk_f16_f32 v159, v86, v87
	ds_read_b64_tr_b16 v[116:117], v65 offset:1024
	ds_read_b64_tr_b16 v[118:119], v65 offset:1536
	s_waitcnt lgkmcnt(11)
	v_mfma_f32_32x32x16_f16 v[96:111], v[180:183], v[136:139], v[96:111]
	v_add_f32_e32 v66, v90, v66
	v_add_f32_e32 v66, v91, v66
	v_add_f32_e32 v66, v92, v66
	v_add_f32_e32 v66, v93, v66
	v_cvt_pk_f16_f32 v152, v88, v89
	v_cvt_pk_f16_f32 v153, v90, v91
	ds_read_b64_tr_b16 v[112:113], v65 offset:5120
	ds_read_b64_tr_b16 v[114:115], v65 offset:5632
	s_waitcnt lgkmcnt(12)
	v_mfma_f32_32x32x16_f16 v[32:47], v[176:179], v[136:139], v[32:47]
	v_add_f32_e32 v66, v94, v66
	v_add_f32_e32 v66, v95, v66
	v_add_f32_e32 v66, v48, v66
	v_add_f32_e32 v66, v49, v66
	v_cvt_pk_f16_f32 v154, v92, v93
	v_cvt_pk_f16_f32 v155, v94, v95
	ds_read_b64_tr_b16 v[92:93], v65 offset:2048
	ds_read_b64_tr_b16 v[94:95], v65 offset:2560
	s_waitcnt lgkmcnt(13)
	v_mfma_f32_32x32x16_f16 v[96:111], v[172:175], v[132:135], v[96:111]
	v_add_f32_e32 v66, v50, v66
	v_add_f32_e32 v66, v51, v66
	v_add_f32_e32 v66, v52, v66
	v_add_f32_e32 v66, v53, v66
	v_cvt_pk_f16_f32 v148, v48, v49
	v_cvt_pk_f16_f32 v149, v50, v51
	ds_read_b64_tr_b16 v[88:89], v65 offset:6144
	ds_read_b64_tr_b16 v[90:91], v65 offset:6656
	s_waitcnt lgkmcnt(14)
	v_mfma_f32_32x32x16_f16 v[32:47], v[168:171], v[132:135], v[32:47]
	v_add_f32_e32 v48, v54, v66
	v_add_f32_e32 v48, v55, v48
	v_add_f32_e32 v48, v56, v48
	v_add_f32_e32 v48, v57, v48
	v_cvt_pk_f16_f32 v150, v52, v53
	v_cvt_pk_f16_f32 v151, v54, v55
	ds_read_b64_tr_b16 v[84:85], v65 offset:3072
	ds_read_b64_tr_b16 v[86:87], v65 offset:3584
	s_waitcnt lgkmcnt(14)
	v_mfma_f32_32x32x16_f16 v[96:111], v[164:167], v[128:131], v[96:111]
	v_add_f32_e32 v48, v58, v48
	v_add_f32_e32 v48, v59, v48
	v_add_f32_e32 v48, v60, v48
	v_add_f32_e32 v48, v61, v48
	v_cvt_pk_f16_f32 v144, v56, v57
	v_cvt_pk_f16_f32 v145, v58, v59
	ds_read_b64_tr_b16 v[80:81], v65 offset:7168
	ds_read_b64_tr_b16 v[82:83], v65 offset:7680
	v_mfma_f32_32x32x16_f16 v[32:47], v[160:163], v[128:131], v[32:47]
	v_add_f32_e32 v48, v62, v48
	v_add_f32_e32 v48, v63, v48
	v_add_f32_e32 v65, 0, v48
	v_cvt_pk_f16_f32 v146, v60, v61
	v_cvt_pk_f16_f32 v147, v62, v63
	s_cmp_lt_u32 s50, 3
	s_cbranch_scc1 .Lmfill_1f
	v_mov_b32_e32 v66, 0xff800000
	v_cmp_le_u32_e32 vcc, v214, v207
	s_mov_b32 s2, 0x41000000
	s_nop 3
	v_cndmask_b32_e32 v32, v66, v32, vcc
	v_cmp_lt_u32_e32 vcc, v213, v207
	s_nop 1
	v_cndmask_b32_e32 v49, v66, v97, vcc
	v_cmp_le_u32_e32 vcc, v213, v207
	s_nop 1
	v_cndmask_b32_e32 v48, v66, v96, vcc
	v_cmp_le_u32_e32 vcc, v215, v207
	v_max_f32_e32 v67, v48, v48
	v_add_f32_e32 v96, v64, v65
	v_cndmask_b32_e32 v33, v66, v33, vcc
	v_cmp_le_u32_e32 vcc, v216, v207
	s_nop 1
	v_cndmask_b32_e32 v50, v66, v98, vcc
	v_cmp_le_u32_e32 vcc, v217, v207
	s_nop 1
	v_cndmask_b32_e32 v34, v66, v34, vcc
	v_cmp_le_u32_e32 vcc, v218, v207
	s_nop 1
	v_cndmask_b32_e32 v51, v66, v99, vcc
	v_cmp_le_u32_e32 vcc, v219, v207
	s_nop 1
	v_cndmask_b32_e32 v35, v66, v35, vcc
	v_cmp_le_u32_e32 vcc, v220, v207
	s_nop 1
	v_cndmask_b32_e32 v52, v66, v100, vcc
	v_cmp_le_u32_e32 vcc, v221, v207
	s_nop 1
	v_cndmask_b32_e32 v36, v66, v36, vcc
	v_cmp_le_u32_e32 vcc, v222, v207
	s_nop 1
	v_cndmask_b32_e32 v53, v66, v101, vcc
	v_cmp_le_u32_e32 vcc, v223, v207
	s_nop 1
	v_cndmask_b32_e32 v37, v66, v37, vcc
	v_cmp_le_u32_e32 vcc, v224, v207
	s_nop 1
	v_cndmask_b32_e32 v54, v66, v102, vcc
	v_cmp_le_u32_e32 vcc, v225, v207
	s_nop 1
	v_cndmask_b32_e32 v38, v66, v38, vcc
	v_cmp_le_u32_e32 vcc, v226, v207
	s_nop 1
	v_cndmask_b32_e32 v55, v66, v103, vcc
	v_cmp_le_u32_e32 vcc, v227, v207
	s_nop 1
	v_cndmask_b32_e32 v39, v66, v39, vcc
	v_cmp_le_u32_e32 vcc, v228, v207
	s_nop 1
	v_cndmask_b32_e32 v56, v66, v104, vcc
	v_cmp_le_u32_e32 vcc, v229, v207
	s_nop 1
	v_cndmask_b32_e32 v40, v66, v40, vcc
	v_cmp_le_u32_e32 vcc, v230, v207
	s_nop 1
	v_cndmask_b32_e32 v57, v66, v105, vcc
	v_cmp_le_u32_e32 vcc, v231, v207
	s_nop 1
	v_cndmask_b32_e32 v41, v66, v41, vcc
	v_cmp_le_u32_e32 vcc, v232, v207
	s_nop 1
	v_cndmask_b32_e32 v58, v66, v106, vcc
	v_cmp_le_u32_e32 vcc, v233, v207
	s_nop 1
	v_cndmask_b32_e32 v42, v66, v42, vcc
	v_cmp_le_u32_e32 vcc, v234, v207
	s_nop 1
	v_cndmask_b32_e32 v59, v66, v107, vcc
	v_cmp_le_u32_e32 vcc, v235, v207
	s_nop 1
	v_cndmask_b32_e32 v43, v66, v43, vcc
	v_cmp_le_u32_e32 vcc, v236, v207
	s_nop 1
	v_cndmask_b32_e32 v60, v66, v108, vcc
	v_cmp_le_u32_e32 vcc, v237, v207
	s_nop 1
	v_cndmask_b32_e32 v44, v66, v44, vcc
	v_cmp_le_u32_e32 vcc, v238, v207
	s_nop 1
	v_cndmask_b32_e32 v61, v66, v109, vcc
	v_cmp_le_u32_e32 vcc, v239, v207
	s_nop 1
	v_cndmask_b32_e32 v45, v66, v45, vcc
	v_cmp_le_u32_e32 vcc, v240, v207
	s_nop 1
	v_cndmask_b32_e32 v62, v66, v110, vcc
	v_cmp_le_u32_e32 vcc, v241, v207
	s_nop 1
	v_cndmask_b32_e32 v46, v66, v46, vcc
	v_cmp_le_u32_e32 vcc, v242, v207
	s_nop 1
	v_cndmask_b32_e32 v63, v66, v111, vcc
	v_cmp_le_u32_e32 vcc, v243, v207
	s_nop 1
	v_cndmask_b32_e32 v47, v66, v47, vcc

.Lfin1_land:
	s_and_saveexec_b64 s[2:3], s[0:1]
	v_add_f32_e32 v32, v65, v32
	ds_write_b32 v205, v32 offset:49280
	s_or_b64 exec, exec, s[2:3]
	s_waitcnt lgkmcnt(0)
	ds_read_b128 v[32:35], v64 offset:49280
	ds_read_b128 v[36:39], v64 offset:49312
	s_add_i32 s0, s20, s29
	s_add_i32 s2, s0, s19
	s_lshl_b32 s0, s28, 6
	s_ashr_i32 s1, s0, 31
	s_waitcnt lgkmcnt(1)
	v_rcp_f32_e32 v40, v32
	s_mul_hi_u32 s3, s2, 0xe80
	s_mulk_i32 s2, 0xe80
	s_add_u32 s2, s10, s2
	v_rcp_f32_e32 v41, v33
	s_addc_u32 s3, s11, s3
	s_lshl_b32 s4, s18, 12
	v_lshl_or_b32 v48, v208, 1, s4
	v_rcp_f32_e32 v42, v34
	v_add_u32_e32 v48, v48, v244
	v_fma_mixlo_f16 v0, v0, v40, 0
	ds_write_b16 v48, v0 offset:51200
	v_fma_mixlo_f16 v0, v16, v40, 0
	v_rcp_f32_e32 v43, v35
	ds_write_b16 v48, v0 offset:51264
	v_fma_mixlo_f16 v0, v1, v41, 0
	ds_write_b16 v48, v0 offset:51328
	v_fma_mixlo_f16 v0, v17, v41, 0
	s_waitcnt lgkmcnt(3)
	v_rcp_f32_e32 v44, v36
	ds_write_b16 v48, v0 offset:51392
	v_fma_mixlo_f16 v0, v2, v42, 0
	ds_write_b16 v48, v0 offset:51456
	v_fma_mixlo_f16 v0, v18, v42, 0
	v_rcp_f32_e32 v45, v37
	ds_write_b16 v48, v0 offset:51520
	v_fma_mixlo_f16 v0, v3, v43, 0
	ds_read_b128 v[32:35], v64 offset:49344
	ds_write_b16 v48, v0 offset:51584
	v_fma_mixlo_f16 v0, v19, v43, 0
	v_rcp_f32_e32 v46, v38
	ds_write_b16 v48, v0 offset:51648
	v_fma_mixlo_f16 v0, v4, v44, 0
	ds_write_b16 v48, v0 offset:52224
	v_fma_mixlo_f16 v0, v20, v44, 0
	v_rcp_f32_e32 v47, v39
	ds_write_b16 v48, v0 offset:52288
	v_fma_mixlo_f16 v0, v5, v45, 0
	ds_write_b16 v48, v0 offset:52352
	v_fma_mixlo_f16 v0, v21, v45, 0
	ds_read_b128 v[36:39], v64 offset:49376
	s_waitcnt lgkmcnt(6)
	v_rcp_f32_e32 v32, v32
	ds_write_b16 v48, v0 offset:52416
	v_fma_mixlo_f16 v0, v6, v46, 0
	ds_write_b16 v48, v0 offset:52480
	v_fma_mixlo_f16 v0, v22, v46, 0
	v_rcp_f32_e32 v33, v33
	ds_write_b16 v48, v0 offset:52544
	v_fma_mixlo_f16 v0, v7, v47, 0
	ds_write_b16 v48, v0 offset:52608
	v_fma_mixlo_f16 v0, v23, v47, 0
	v_rcp_f32_e32 v34, v34
	ds_write_b16 v48, v0 offset:52672
	v_fma_mixlo_f16 v0, v8, v32, 0
	ds_write_b16 v48, v0 offset:53248
	v_fma_mixlo_f16 v0, v24, v32, 0
	v_rcp_f32_e32 v35, v35
	ds_write_b16 v48, v0 offset:53312
	v_fma_mixlo_f16 v0, v9, v33, 0
	ds_write_b16 v48, v0 offset:53376
	v_fma_mixlo_f16 v0, v25, v33, 0
	s_waitcnt lgkmcnt(8)
	v_rcp_f32_e32 v36, v36
	ds_write_b16 v48, v0 offset:53440
	v_fma_mixlo_f16 v0, v10, v34, 0
	ds_write_b16 v48, v0 offset:53504
	v_fma_mixlo_f16 v0, v26, v34, 0
	v_rcp_f32_e32 v37, v37
	ds_write_b16 v48, v0 offset:53568
	v_fma_mixlo_f16 v0, v11, v35, 0
	ds_write_b16 v48, v0 offset:53632
	v_fma_mixlo_f16 v0, v27, v35, 0
	v_rcp_f32_e32 v38, v38
	ds_write_b16 v48, v0 offset:53696
	v_fma_mixlo_f16 v0, v12, v36, 0
	ds_write_b16 v48, v0 offset:54272
	v_fma_mixlo_f16 v0, v28, v36, 0
	v_rcp_f32_e32 v39, v39
	ds_write_b16 v48, v0 offset:54336
	v_fma_mixlo_f16 v0, v13, v37, 0
	ds_write_b16 v48, v0 offset:54400
	v_fma_mixlo_f16 v0, v29, v37, 0
	ds_write_b16 v48, v0 offset:54464
	v_fma_mixlo_f16 v0, v14, v38, 0
	ds_write_b16 v48, v0 offset:54528
	v_fma_mixlo_f16 v0, v30, v38, 0
	ds_write_b16 v48, v0 offset:54592
	v_fma_mixlo_f16 v0, v15, v39, 0
	ds_write_b16 v48, v0 offset:54656
	v_fma_mixlo_f16 v0, v31, v39, 0
	s_lshl_b64 s[0:1], s[0:1], 1
	ds_write_b16 v48, v0 offset:54720
	s_add_u32 s0, s2, s0
	v_or_b32_e32 v12, s4, v204
	s_addc_u32 s1, s3, s1
	s_waitcnt lgkmcnt(0)
	v_mov_b32_e32 v205, 0
	v_add_u32_e32 v0, v12, v245
	v_lshl_add_u64 v[4:5], s[0:1], 0, v[204:205]
	ds_read_b128 v[0:3], v0 offset:51200
	v_mov_b32_e32 v207, v205
	v_lshl_add_u64 v[8:9], v[4:5], 0, v[206:207]
	v_add_u32_e32 v4, v12, v246
	ds_read_b128 v[4:7], v4 offset:51200
	s_movk_i32 s0, 0x7000
	s_waitcnt lgkmcnt(1)
	global_store_dwordx4 v[8:9], v[0:3], off sc0 sc1
	s_nop 1
	v_add_co_u32_e32 v0, vcc, s0, v8
	s_nop 1
	v_addc_co_u32_e32 v1, vcc, 0, v9, vcc
	s_waitcnt lgkmcnt(0)
	global_store_dwordx4 v[0:1], v[4:7], off offset:1024 sc0 sc1
	v_add_u32_e32 v0, v12, v247
	ds_read_b128 v[0:3], v0 offset:51200
	v_add_u32_e32 v4, v12, v248
	ds_read_b128 v[4:7], v4 offset:51200
	v_add_co_u32_e32 v10, vcc, 0xe000, v8
	s_nop 1
	v_addc_co_u32_e32 v11, vcc, 0, v9, vcc
	s_waitcnt lgkmcnt(1)
	global_store_dwordx4 v[10:11], v[0:3], off offset:2048 sc0 sc1
	s_nop 1
	v_add_co_u32_e32 v0, vcc, 0x15000, v8
	s_nop 1
	v_addc_co_u32_e32 v1, vcc, 0, v9, vcc
	s_waitcnt lgkmcnt(0)
	global_store_dwordx4 v[0:1], v[4:7], off offset:3072 sc0 sc1
	s_waitcnt lgkmcnt(0)
	s_barrier

.Lfin0_skip:
	s_nop 7
	s_nop 3
	v_mov_b32_e32 v34, 0
	v_mov_b32_e32 v35, 0
	v_mov_b32_e32 v36, 0
	v_mov_b32_e32 v37, 0
	v_mov_b32_e32 v38, 0
	v_mov_b32_e32 v39, 0
	v_mov_b32_e32 v40, 0
	v_mov_b32_e32 v41, 0
	v_mov_b32_e32 v42, 0
	v_mov_b32_e32 v43, 0
	v_mov_b32_e32 v44, 0
	v_mov_b32_e32 v45, 0
	v_mov_b32_e32 v46, 0
	v_mov_b32_e32 v47, 0
	v_mov_b32_e32 v48, 0
	v_mov_b32_e32 v49, 0
	v_mov_b32_e32 v50, 0
	v_mov_b32_e32 v51, 0
	v_mov_b32_e32 v52, 0
	v_mov_b32_e32 v53, 0
	v_mov_b32_e32 v54, 0
	v_mov_b32_e32 v55, 0
	v_mov_b32_e32 v56, 0
	v_mov_b32_e32 v57, 0
	v_mov_b32_e32 v58, 0
	v_mov_b32_e32 v59, 0
	v_mov_b32_e32 v60, 0
	v_mov_b32_e32 v61, 0
	v_mov_b32_e32 v62, 0
	v_mov_b32_e32 v63, 0
	v_mov_b32_e32 v64, 0
	v_mov_b32_e32 v65, 0
	v_mov_b32_e32 v82, v203
	v_lshl_add_u32 v66, v210, 2, s38
	s_mov_b32 s3, 0
	s_cmp_lt_i32 s36, 0
	s_branch .Lfin0_land
.Lfin1_skip:
	s_nop 7
	s_nop 3
	v_mov_b32_e32 v65, v64
	v_lshl_add_u32 v64, v210, 2, s21
	v_mov_b32_e32 v32, v65
	s_nop 1
	v_permlane32_swap_b32_e32 v65, v32
	s_branch .Lfin1_land
	.p2align	8
